# step body regenerated (2 z buffers, 16-wide chains, first accumulate pass folded into sigmoid stream); s_setprio 3 from flush start until next step
# speedup vs baseline: 1.0657x; 1.0174x over previous
.LBB1_141:
	s_or_b64 exec, exec, s[6:7]
	v_and_b32_e32 v1, 31, v0
	s_waitcnt lgkmcnt(0)
	v_lshlrev_b32_e32 v2, 2, v1
	v_or_b32_e32 v22, 32, v8
	s_barrier
	v_readfirstlane_b32 s95, v9
	s_cmp_lt_u32 s95, 4
	s_cbranch_scc1 .Lstag_done
	s_nop 0

.LBB1_145:
	s_setprio 0
	s_waitcnt vmcnt(0)
	v_cvt_f16_f32_e32 v1, v241
	v_cvt_pk_f16_f32 v194, v241, v241
	v_add_lshl_u32 v0, s13, v240, 1
	v_lshl_or_b32 v4, v236, 3, 3
	v_cvt_f32_f16_e32 v3, v1
	v_ashrrev_i32_e32 v1, 31, v0
	v_cmp_gt_u32_e32 vcc, s14, v236
	v_mov_b32_e32 v5, v2
	v_sub_f32_e32 v3, v241, v3
	v_cvt_f16_f32_e32 v3, v3
	v_cndmask_b32_e32 v4, 3, v4, vcc
	v_lshl_add_u64 v[6:7], v[0:1], 2, v[232:233]
	v_lshl_add_u64 v[4:5], v[4:5], 2, s[54:55]
	v_perm_b32 v195, v196, v3, s15
	flat_load_dwordx2 v[0:1], v[6:7]
	global_load_dword v241, v[4:5], off
	s_add_i32 s18, s13, 32
	s_add_i32 s19, s13, 16
	s_mov_b64 s[6:7], 0
	v_mfma_f32_32x32x16_f16 v[82:97], v[194:197], v[178:181], 0
	v_mfma_f32_32x32x16_f16 v[98:113], v[194:197], v[182:185], 0
	v_add_u32_e32 v14, s13, v243
	v_sub_u32_e32 v3, v230, v14
	v_max_i32_e32 v4, 0, v3
	v_add_u32_e32 v3, v3, v234
	v_min_i32_e32 v3, 32, v3
	v_sub_u32_e32 v3, v3, v4
	v_max_i32_e32 v3, 0, v3
	v_min_i32_e32 v15, 32, v4
	v_lshlrev_b64 v[4:5], v3, -1
	v_not_b32_e32 v4, v4
	v_lshlrev_b64 v[4:5], v15, v[4:5]
	v_and_b32_e32 v3, 1, v4
	v_lshlrev_b32_e32 v5, 15, v4
	v_and_or_b32 v3, v5, s16, v3
	v_mul_u32_u24_e32 v6, 0x3c00, v3
	v_bfe_u32 v3, v4, 2, 1
	v_lshlrev_b32_e32 v5, 13, v4
	v_and_or_b32 v3, v5, s16, v3
	v_mul_u32_u24_e32 v7, 0x3c00, v3
	v_bfe_u32 v3, v4, 8, 1
	v_lshlrev_b32_e32 v5, 7, v4
	v_and_or_b32 v3, v5, s16, v3
	v_mul_u32_u24_e32 v8, 0x3c00, v3
	v_bfe_u32 v3, v4, 10, 1
	v_lshlrev_b32_e32 v5, 5, v4
	v_and_or_b32 v3, v5, s16, v3
	v_mul_u32_u24_e32 v9, 0x3c00, v3
	v_bfe_u32 v3, v4, 16, 1
	v_lshrrev_b32_e32 v5, 1, v4
	v_and_or_b32 v3, v5, s16, v3
	v_mul_u32_u24_e32 v10, 0x3c00, v3
	v_bfe_u32 v3, v4, 18, 1
	v_lshrrev_b32_e32 v5, 3, v4
	v_and_or_b32 v3, v5, s16, v3
	v_mul_u32_u24_e32 v11, 0x3c00, v3
	v_bfe_u32 v3, v4, 24, 1
	v_lshrrev_b32_e32 v5, 9, v4
	v_and_or_b32 v3, v5, s16, v3
	v_mul_u32_u24_e32 v12, 0x3c00, v3
	v_bfe_u32 v3, v4, 26, 1
	v_lshrrev_b32_e32 v5, 11, v4
	v_and_or_b32 v3, v5, s16, v3
	v_mul_u32_u24_e32 v13, 0x3c00, v3
	v_exp_f32_e32 v82, v82
	v_exp_f32_e32 v83, v83
	v_exp_f32_e32 v84, v84
	v_exp_f32_e32 v85, v85
	v_exp_f32_e32 v86, v86
	v_exp_f32_e32 v87, v87
	v_exp_f32_e32 v88, v88
	v_exp_f32_e32 v89, v89
	v_exp_f32_e32 v90, v90
	v_exp_f32_e32 v91, v91
	v_exp_f32_e32 v92, v92
	v_exp_f32_e32 v93, v93
	v_exp_f32_e32 v94, v94
	v_exp_f32_e32 v95, v95
	v_exp_f32_e32 v96, v96
	v_exp_f32_e32 v97, v97
	v_add_f32_e32 v82, 1.0, v82
	v_add_f32_e32 v83, 1.0, v83
	v_add_f32_e32 v84, 1.0, v84
	v_add_f32_e32 v85, 1.0, v85
	v_add_f32_e32 v86, 1.0, v86
	v_add_f32_e32 v87, 1.0, v87
	v_add_f32_e32 v88, 1.0, v88
	v_add_f32_e32 v89, 1.0, v89
	v_add_f32_e32 v90, 1.0, v90
	v_add_f32_e32 v91, 1.0, v91
	v_add_f32_e32 v92, 1.0, v92
	v_add_f32_e32 v93, 1.0, v93
	v_add_f32_e32 v94, 1.0, v94
	v_add_f32_e32 v95, 1.0, v95
	v_add_f32_e32 v96, 1.0, v96
	v_add_f32_e32 v97, 1.0, v97
	v_rcp_f32_e32 v82, v82
	v_rcp_f32_e32 v83, v83
	v_rcp_f32_e32 v84, v84
	v_rcp_f32_e32 v85, v85
	v_rcp_f32_e32 v86, v86
	v_rcp_f32_e32 v87, v87
	v_rcp_f32_e32 v88, v88
	v_rcp_f32_e32 v89, v89
	v_rcp_f32_e32 v90, v90
	v_rcp_f32_e32 v91, v91
	v_rcp_f32_e32 v92, v92
	v_rcp_f32_e32 v93, v93
	v_rcp_f32_e32 v94, v94
	v_rcp_f32_e32 v95, v95
	v_rcp_f32_e32 v96, v96
	v_rcp_f32_e32 v97, v97
	v_cvt_pk_f16_f32 v198, v82, v83
	v_cvt_pk_f16_f32 v199, v84, v85
	v_cvt_pk_f16_f32 v200, v86, v87
	v_cvt_pk_f16_f32 v201, v88, v89
	v_cvt_pk_f16_f32 v202, v90, v91
	v_cvt_pk_f16_f32 v203, v92, v93
	v_cvt_pk_f16_f32 v204, v94, v95
	v_cvt_pk_f16_f32 v205, v96, v97
	v_mfma_f32_32x32x16_f16 v[82:97], v[194:197], v[186:189], 0
	v_exp_f32_e32 v98, v98
	v_exp_f32_e32 v99, v99
	v_exp_f32_e32 v100, v100
	v_exp_f32_e32 v101, v101
	v_exp_f32_e32 v102, v102
	v_exp_f32_e32 v103, v103
	v_mfma_f32_32x32x16_f16 v[66:81], v[198:201], v[6:9], v[66:81]
	v_exp_f32_e32 v104, v104
	v_exp_f32_e32 v105, v105
	v_exp_f32_e32 v106, v106
	v_exp_f32_e32 v107, v107
	v_exp_f32_e32 v108, v108
	v_exp_f32_e32 v109, v109
	v_mfma_f32_32x32x16_f16 v[66:81], v[202:205], v[10:13], v[66:81]
	v_exp_f32_e32 v110, v110
	v_exp_f32_e32 v111, v111
	v_exp_f32_e32 v112, v112
	v_exp_f32_e32 v113, v113
	v_add_f32_e32 v98, 1.0, v98
	v_add_f32_e32 v99, 1.0, v99
	v_add_f32_e32 v100, 1.0, v100
	v_add_f32_e32 v101, 1.0, v101
	v_add_f32_e32 v102, 1.0, v102
	v_add_f32_e32 v103, 1.0, v103
	v_add_f32_e32 v104, 1.0, v104
	v_add_f32_e32 v105, 1.0, v105
	v_add_f32_e32 v106, 1.0, v106
	v_add_f32_e32 v107, 1.0, v107
	v_add_f32_e32 v108, 1.0, v108
	v_add_f32_e32 v109, 1.0, v109
	v_add_f32_e32 v110, 1.0, v110
	v_add_f32_e32 v111, 1.0, v111
	v_add_f32_e32 v112, 1.0, v112
	v_add_f32_e32 v113, 1.0, v113
	v_rcp_f32_e32 v98, v98
	v_rcp_f32_e32 v99, v99
	v_rcp_f32_e32 v100, v100
	v_rcp_f32_e32 v101, v101
	v_rcp_f32_e32 v102, v102
	v_rcp_f32_e32 v103, v103
	v_rcp_f32_e32 v104, v104
	v_rcp_f32_e32 v105, v105
	v_rcp_f32_e32 v106, v106
	v_rcp_f32_e32 v107, v107
	v_rcp_f32_e32 v108, v108
	v_rcp_f32_e32 v109, v109
	v_rcp_f32_e32 v110, v110
	v_rcp_f32_e32 v111, v111
	v_rcp_f32_e32 v112, v112
	v_rcp_f32_e32 v113, v113
	v_cvt_pk_f16_f32 v206, v98, v99
	v_cvt_pk_f16_f32 v207, v100, v101
	v_cvt_pk_f16_f32 v208, v102, v103
	v_cvt_pk_f16_f32 v209, v104, v105
	v_cvt_pk_f16_f32 v210, v106, v107
	v_cvt_pk_f16_f32 v211, v108, v109
	v_cvt_pk_f16_f32 v212, v110, v111
	v_cvt_pk_f16_f32 v213, v112, v113
	v_mfma_f32_32x32x16_f16 v[98:113], v[194:197], v[190:193], 0
	v_exp_f32_e32 v82, v82
	v_exp_f32_e32 v83, v83
	v_exp_f32_e32 v84, v84
	v_exp_f32_e32 v85, v85
	v_exp_f32_e32 v86, v86
	v_exp_f32_e32 v87, v87
	v_mfma_f32_32x32x16_f16 v[50:65], v[206:209], v[6:9], v[50:65]
	v_exp_f32_e32 v88, v88
	v_exp_f32_e32 v89, v89
	v_exp_f32_e32 v90, v90
	v_exp_f32_e32 v91, v91
	v_exp_f32_e32 v92, v92
	v_exp_f32_e32 v93, v93
	v_mfma_f32_32x32x16_f16 v[50:65], v[210:213], v[10:13], v[50:65]
	v_exp_f32_e32 v94, v94
	v_exp_f32_e32 v95, v95
	v_exp_f32_e32 v96, v96
	v_exp_f32_e32 v97, v97
	v_add_f32_e32 v82, 1.0, v82
	v_add_f32_e32 v83, 1.0, v83
	v_add_f32_e32 v84, 1.0, v84
	v_add_f32_e32 v85, 1.0, v85
	v_add_f32_e32 v86, 1.0, v86
	v_add_f32_e32 v87, 1.0, v87
	v_add_f32_e32 v88, 1.0, v88
	v_add_f32_e32 v89, 1.0, v89
	v_add_f32_e32 v90, 1.0, v90
	v_add_f32_e32 v91, 1.0, v91
	v_add_f32_e32 v92, 1.0, v92
	v_add_f32_e32 v93, 1.0, v93
	v_add_f32_e32 v94, 1.0, v94
	v_add_f32_e32 v95, 1.0, v95
	v_add_f32_e32 v96, 1.0, v96
	v_add_f32_e32 v97, 1.0, v97
	v_rcp_f32_e32 v82, v82
	v_rcp_f32_e32 v83, v83
	v_rcp_f32_e32 v84, v84
	v_rcp_f32_e32 v85, v85
	v_rcp_f32_e32 v86, v86
	v_rcp_f32_e32 v87, v87
	v_rcp_f32_e32 v88, v88
	v_rcp_f32_e32 v89, v89
	v_rcp_f32_e32 v90, v90
	v_rcp_f32_e32 v91, v91
	v_rcp_f32_e32 v92, v92
	v_rcp_f32_e32 v93, v93
	v_rcp_f32_e32 v94, v94
	v_rcp_f32_e32 v95, v95
	v_rcp_f32_e32 v96, v96
	v_rcp_f32_e32 v97, v97
	v_cvt_pk_f16_f32 v214, v82, v83
	v_cvt_pk_f16_f32 v215, v84, v85
	v_cvt_pk_f16_f32 v216, v86, v87
	v_cvt_pk_f16_f32 v217, v88, v89
	v_cvt_pk_f16_f32 v218, v90, v91
	v_cvt_pk_f16_f32 v219, v92, v93
	v_cvt_pk_f16_f32 v220, v94, v95
	v_cvt_pk_f16_f32 v221, v96, v97
	v_exp_f32_e32 v98, v98
	v_exp_f32_e32 v99, v99
	v_exp_f32_e32 v100, v100
	v_exp_f32_e32 v101, v101
	v_exp_f32_e32 v102, v102
	v_exp_f32_e32 v103, v103
	v_mfma_f32_32x32x16_f16 v[34:49], v[214:217], v[6:9], v[34:49]
	v_exp_f32_e32 v104, v104
	v_exp_f32_e32 v105, v105
	v_exp_f32_e32 v106, v106
	v_exp_f32_e32 v107, v107
	v_exp_f32_e32 v108, v108
	v_exp_f32_e32 v109, v109
	v_mfma_f32_32x32x16_f16 v[34:49], v[218:221], v[10:13], v[34:49]
	v_exp_f32_e32 v110, v110
	v_exp_f32_e32 v111, v111
	v_exp_f32_e32 v112, v112
	v_exp_f32_e32 v113, v113
	v_add_f32_e32 v98, 1.0, v98
	v_add_f32_e32 v99, 1.0, v99
	v_add_f32_e32 v100, 1.0, v100
	v_add_f32_e32 v101, 1.0, v101
	v_add_f32_e32 v102, 1.0, v102
	v_add_f32_e32 v103, 1.0, v103
	v_add_f32_e32 v104, 1.0, v104
	v_add_f32_e32 v105, 1.0, v105
	v_add_f32_e32 v106, 1.0, v106
	v_add_f32_e32 v107, 1.0, v107
	v_add_f32_e32 v108, 1.0, v108
	v_add_f32_e32 v109, 1.0, v109
	v_add_f32_e32 v110, 1.0, v110
	v_add_f32_e32 v111, 1.0, v111
	v_add_f32_e32 v112, 1.0, v112
	v_add_f32_e32 v113, 1.0, v113
	v_rcp_f32_e32 v98, v98
	v_rcp_f32_e32 v99, v99
	v_rcp_f32_e32 v100, v100
	v_rcp_f32_e32 v101, v101
	v_rcp_f32_e32 v102, v102
	v_rcp_f32_e32 v103, v103
	v_rcp_f32_e32 v104, v104
	v_rcp_f32_e32 v105, v105
	v_rcp_f32_e32 v106, v106
	v_rcp_f32_e32 v107, v107
	v_rcp_f32_e32 v108, v108
	v_rcp_f32_e32 v109, v109
	v_rcp_f32_e32 v110, v110
	v_rcp_f32_e32 v111, v111
	v_rcp_f32_e32 v112, v112
	v_rcp_f32_e32 v113, v113
	v_cvt_pk_f16_f32 v222, v98, v99
	v_cvt_pk_f16_f32 v223, v100, v101
	v_cvt_pk_f16_f32 v224, v102, v103
	v_cvt_pk_f16_f32 v225, v104, v105
	v_cvt_pk_f16_f32 v226, v106, v107
	v_cvt_pk_f16_f32 v227, v108, v109
	v_cvt_pk_f16_f32 v228, v110, v111
	v_cvt_pk_f16_f32 v229, v112, v113
	v_mfma_f32_32x32x16_f16 v[18:33], v[222:225], v[6:9], v[18:33]
	v_add_u32_e32 v194, s13, v243
	v_mfma_f32_32x32x16_f16 v[18:33], v[226:229], v[10:13], v[18:33]
	s_branch .Lpeel_join

.Lpeel_join:
	v_cmp_ge_i32_e32 vcc, s18, v249
	s_mov_b64 s[8:9], 0
	s_and_saveexec_b64 s[2:3], vcc
	s_cbranch_execz .LBB1_148
	s_setprio 3
	v_cmp_gt_i32_e32 vcc, s12, v235
	s_and_b64 s[10:11], s[0:1], vcc
	ds_read_b128 v[82:85], v245 offset:32768
	ds_read_b128 v[86:89], v245 offset:32784
	ds_read_b128 v[90:93], v245 offset:32800
	ds_read_b128 v[94:97], v245 offset:32816
	ds_read_b128 v[98:101], v245 offset:32832
	ds_read_b128 v[102:105], v245 offset:32848
	ds_read_b128 v[106:109], v245 offset:32864
	ds_read_b128 v[110:113], v245 offset:32880
	ds_read_b128 v[114:117], v246 offset:0
	ds_read_b128 v[118:121], v246 offset:8192
	ds_read_b128 v[122:125], v246 offset:1024
	ds_read_b128 v[126:129], v246 offset:9216
	v_cvt_f32_i32_e32 v16, v234
	v_cvt_pk_f16_f32 v4, v66, v67
	v_cvt_pk_f16_f32 v5, v68, v69
	v_cvt_pk_f16_f32 v6, v70, v71
	v_cvt_pk_f16_f32 v7, v72, v73
	v_cvt_pk_f16_f32 v8, v74, v75
	v_cvt_pk_f16_f32 v9, v76, v77
	v_cvt_pk_f16_f32 v10, v78, v79
	v_cvt_pk_f16_f32 v11, v80, v81
	s_waitcnt lgkmcnt(8)
	v_pk_mul_f32 v[162:163], v[82:83], v[16:17] op_sel_hi:[1,0]
	v_pk_mul_f32 v[164:165], v[84:85], v[16:17] op_sel_hi:[1,0]
	v_pk_mul_f32 v[166:167], v[86:87], v[16:17] op_sel_hi:[1,0]
	v_pk_mul_f32 v[168:169], v[88:89], v[16:17] op_sel_hi:[1,0]
	v_pk_mul_f32 v[170:171], v[90:91], v[16:17] op_sel_hi:[1,0]
	v_pk_mul_f32 v[172:173], v[92:93], v[16:17] op_sel_hi:[1,0]
	v_pk_mul_f32 v[174:175], v[94:95], v[16:17] op_sel_hi:[1,0]
	v_pk_mul_f32 v[176:177], v[96:97], v[16:17] op_sel_hi:[1,0]
	ds_read_b128 v[130:133], v246 offset:2048
	ds_read_b128 v[134:137], v246 offset:10240
	ds_read_b128 v[138:141], v246 offset:3072
	ds_read_b128 v[142:145], v246 offset:11264
	s_waitcnt lgkmcnt(4)
	v_mfma_f32_32x32x16_f16 v[162:177], v[114:117], v[4:7], v[162:177]
	v_pk_mul_f32 v[146:147], v[98:99], v[16:17] op_sel_hi:[1,0]
	v_pk_mul_f32 v[148:149], v[100:101], v[16:17] op_sel_hi:[1,0]
	v_pk_mul_f32 v[150:151], v[102:103], v[16:17] op_sel_hi:[1,0]
	v_pk_mul_f32 v[152:153], v[104:105], v[16:17] op_sel_hi:[1,0]
	v_pk_mul_f32 v[154:155], v[106:107], v[16:17] op_sel_hi:[1,0]
	v_pk_mul_f32 v[156:157], v[108:109], v[16:17] op_sel_hi:[1,0]
	v_pk_mul_f32 v[158:159], v[110:111], v[16:17] op_sel_hi:[1,0]
	v_pk_mul_f32 v[160:161], v[112:113], v[16:17] op_sel_hi:[1,0]
	s_nop 1
	v_mfma_f32_32x32x16_f16 v[146:161], v[118:121], v[4:7], v[146:161]
	v_cvt_pk_f16_f32 v12, v50, v51
	v_cvt_pk_f16_f32 v13, v52, v53
	v_cvt_pk_f16_f32 v14, v54, v55
	v_cvt_pk_f16_f32 v15, v56, v57
	v_mfma_f32_32x32x16_f16 v[162:177], v[122:125], v[8:11], v[162:177]
	v_cvt_pk_f16_f32 v252, v58, v59
	v_cvt_pk_f16_f32 v253, v60, v61
	v_cvt_pk_f16_f32 v254, v62, v63
	v_cvt_pk_f16_f32 v255, v64, v65
	v_mfma_f32_32x32x16_f16 v[146:161], v[126:129], v[8:11], v[146:161]
	ds_read_b128 v[82:85], v246 offset:4096
	ds_read_b128 v[86:89], v246 offset:12288
	ds_read_b128 v[90:93], v246 offset:5120
	ds_read_b128 v[94:97], v246 offset:13312
	s_waitcnt lgkmcnt(4)
	v_mfma_f32_32x32x16_f16 v[162:177], v[130:133], v[12:15], v[162:177]
	v_cvt_pk_f16_f32 v4, v34, v35
	v_cvt_pk_f16_f32 v5, v36, v37
	v_mfma_f32_32x32x16_f16 v[146:161], v[134:137], v[12:15], v[146:161]
	v_cvt_pk_f16_f32 v6, v38, v39
	v_cvt_pk_f16_f32 v7, v40, v41
	v_mfma_f32_32x32x16_f16 v[162:177], v[138:141], v[252:255], v[162:177]
	v_cvt_pk_f16_f32 v8, v42, v43
	v_cvt_pk_f16_f32 v9, v44, v45
	v_mfma_f32_32x32x16_f16 v[146:161], v[142:145], v[252:255], v[146:161]
	v_cvt_pk_f16_f32 v10, v46, v47
	v_cvt_pk_f16_f32 v11, v48, v49
	ds_read_b128 v[98:101], v246 offset:6144
	ds_read_b128 v[102:105], v246 offset:14336
	ds_read_b128 v[106:109], v246 offset:7168
	ds_read_b128 v[110:113], v246 offset:15360
	s_waitcnt lgkmcnt(4)
	v_mfma_f32_32x32x16_f16 v[162:177], v[82:85], v[4:7], v[162:177]
	v_cvt_pk_f16_f32 v12, v18, v19
	v_cvt_pk_f16_f32 v13, v20, v21
	v_mfma_f32_32x32x16_f16 v[146:161], v[86:89], v[4:7], v[146:161]
	v_cvt_pk_f16_f32 v14, v22, v23
	v_cvt_pk_f16_f32 v15, v24, v25
	v_mfma_f32_32x32x16_f16 v[162:177], v[90:93], v[8:11], v[162:177]
	v_cvt_pk_f16_f32 v252, v26, v27
	v_cvt_pk_f16_f32 v253, v28, v29
	v_mfma_f32_32x32x16_f16 v[146:161], v[94:97], v[8:11], v[146:161]
	v_cvt_pk_f16_f32 v254, v30, v31
	v_cvt_pk_f16_f32 v255, v32, v33
	ds_read_b128 v[18:21], v246 offset:16384
	ds_read_b128 v[22:25], v246 offset:17408
	ds_read_b128 v[26:29], v246 offset:18432
	ds_read_b128 v[30:33], v246 offset:19456
	s_waitcnt lgkmcnt(4)
	v_mfma_f32_32x32x16_f16 v[162:177], v[98:101], v[12:15], v[162:177]
	v_mfma_f32_32x32x16_f16 v[146:161], v[102:105], v[12:15], v[146:161]
	v_mfma_f32_32x32x16_f16 v[162:177], v[106:109], v[252:255], v[162:177]
	v_mfma_f32_32x32x16_f16 v[146:161], v[110:113], v[252:255], v[146:161]
	ds_read_b128 v[130:133], v247 offset:33024
	ds_read_b128 v[134:137], v247 offset:33040
	ds_read_b128 v[138:141], v247 offset:33056
	ds_read_b128 v[142:145], v247 offset:33072
	ds_read_b128 v[114:117], v247 offset:33088
	ds_read_b128 v[118:121], v247 offset:33104
	ds_read_b128 v[122:125], v247 offset:33120
	ds_read_b128 v[126:129], v247 offset:33136
	s_nop 2
	v_cvt_pk_f16_f32 v4, v162, v163
	v_cvt_pk_f16_f32 v5, v164, v165
	v_cvt_pk_f16_f32 v6, v166, v167
	v_cvt_pk_f16_f32 v7, v168, v169
	v_cvt_pk_f16_f32 v8, v170, v171
	v_cvt_pk_f16_f32 v9, v172, v173
	v_cvt_pk_f16_f32 v10, v174, v175
	v_cvt_pk_f16_f32 v11, v176, v177
	v_cvt_pk_f16_f32 v12, v146, v147
	v_cvt_pk_f16_f32 v13, v148, v149
	v_cvt_pk_f16_f32 v14, v150, v151
	v_cvt_pk_f16_f32 v15, v152, v153
	v_cvt_pk_f16_f32 v252, v154, v155
	v_cvt_pk_f16_f32 v253, v156, v157
	v_cvt_pk_f16_f32 v254, v158, v159
	v_cvt_pk_f16_f32 v255, v160, v161
	s_waitcnt lgkmcnt(4)
	ds_read_b128 v[34:37], v246 offset:20480
	ds_read_b128 v[38:41], v246 offset:21504
	ds_read_b128 v[42:45], v246 offset:22528
	ds_read_b128 v[46:49], v246 offset:23552
	v_mfma_f32_32x32x16_f16 v[130:145], v[18:21], v[4:7], v[130:145]
	v_mfma_f32_32x32x16_f16 v[130:145], v[22:25], v[8:11], v[130:145]
	v_mfma_f32_32x32x16_f16 v[130:145], v[26:29], v[12:15], v[130:145]
	v_mfma_f32_32x32x16_f16 v[130:145], v[30:33], v[252:255], v[130:145]
	ds_read_b128 v[146:149], v247 offset:33536
	ds_read_b128 v[150:153], v247 offset:33552
	ds_read_b128 v[154:157], v247 offset:33568
	ds_read_b128 v[158:161], v247 offset:33584
	s_waitcnt lgkmcnt(4)
	ds_read_b128 v[98:101], v247 offset:33152
	ds_read_b128 v[102:105], v247 offset:33168
	ds_read_b128 v[106:109], v247 offset:33184
	ds_read_b128 v[110:113], v247 offset:33200
	ds_read_b128 v[50:53], v246 offset:24576
	ds_read_b128 v[54:57], v246 offset:25600
	ds_read_b128 v[58:61], v246 offset:26624
	ds_read_b128 v[62:65], v246 offset:27648
	v_mfma_f32_32x32x16_f16 v[114:129], v[34:37], v[4:7], v[114:129]
	v_exp_f32_e32 v130, v130
	v_exp_f32_e32 v131, v131
	v_exp_f32_e32 v132, v132
	v_exp_f32_e32 v133, v133
	v_exp_f32_e32 v134, v134
	v_exp_f32_e32 v135, v135
	v_exp_f32_e32 v136, v136
	v_exp_f32_e32 v137, v137
	v_mfma_f32_32x32x16_f16 v[114:129], v[38:41], v[8:11], v[114:129]
	v_exp_f32_e32 v138, v138
	v_exp_f32_e32 v139, v139
	v_exp_f32_e32 v140, v140
	v_exp_f32_e32 v141, v141
	v_exp_f32_e32 v142, v142
	v_exp_f32_e32 v143, v143
	v_exp_f32_e32 v144, v144
	v_exp_f32_e32 v145, v145
	v_mfma_f32_32x32x16_f16 v[114:129], v[42:45], v[12:15], v[114:129]
	v_add_f32_e32 v130, 1.0, v130
	v_add_f32_e32 v131, 1.0, v131
	v_add_f32_e32 v132, 1.0, v132
	v_add_f32_e32 v133, 1.0, v133
	v_add_f32_e32 v134, 1.0, v134
	v_add_f32_e32 v135, 1.0, v135
	v_add_f32_e32 v136, 1.0, v136
	v_add_f32_e32 v137, 1.0, v137
	v_add_f32_e32 v138, 1.0, v138
	v_add_f32_e32 v139, 1.0, v139
	v_add_f32_e32 v140, 1.0, v140
	v_add_f32_e32 v141, 1.0, v141
	v_add_f32_e32 v142, 1.0, v142
	v_add_f32_e32 v143, 1.0, v143
	v_add_f32_e32 v144, 1.0, v144
	v_add_f32_e32 v145, 1.0, v145
	v_mfma_f32_32x32x16_f16 v[114:129], v[46:49], v[252:255], v[114:129]
	v_rcp_f32_e32 v130, v130
	v_rcp_f32_e32 v131, v131
	v_rcp_f32_e32 v132, v132
	v_rcp_f32_e32 v133, v133
	v_rcp_f32_e32 v134, v134
	v_rcp_f32_e32 v135, v135
	v_rcp_f32_e32 v136, v136
	v_rcp_f32_e32 v137, v137
	v_rcp_f32_e32 v138, v138
	v_rcp_f32_e32 v139, v139
	v_rcp_f32_e32 v140, v140
	v_rcp_f32_e32 v141, v141
	v_rcp_f32_e32 v142, v142
	v_rcp_f32_e32 v143, v143
	v_rcp_f32_e32 v144, v144
	v_rcp_f32_e32 v145, v145
	s_waitcnt lgkmcnt(8)
	ds_read_b128 v[162:165], v247 offset:33600
	ds_read_b128 v[166:169], v247 offset:33616
	ds_read_b128 v[170:173], v247 offset:33632
	ds_read_b128 v[174:177], v247 offset:33648
	v_mul_f32_e32 v3, v146, v130
	v_mul_f32_e32 v16, v147, v131
	v_mul_f32_e32 v17, v148, v132
	v_fmac_f32_e32 v3, v149, v133
	v_fmac_f32_e32 v16, v150, v134
	v_fmac_f32_e32 v17, v151, v135
	v_fmac_f32_e32 v3, v152, v136
	v_fmac_f32_e32 v16, v153, v137
	v_fmac_f32_e32 v17, v154, v138
	v_fmac_f32_e32 v3, v155, v139
	v_fmac_f32_e32 v16, v156, v140
	v_fmac_f32_e32 v17, v157, v141
	v_fmac_f32_e32 v3, v158, v142
	v_fmac_f32_e32 v16, v159, v143
	v_fmac_f32_e32 v17, v160, v144
	v_fmac_f32_e32 v3, v161, v145
	s_waitcnt lgkmcnt(4)
	ds_read_b128 v[82:85], v247 offset:33216
	ds_read_b128 v[86:89], v247 offset:33232
	ds_read_b128 v[90:93], v247 offset:33248
	ds_read_b128 v[94:97], v247 offset:33264
	ds_read_b128 v[66:69], v246 offset:28672
	ds_read_b128 v[70:73], v246 offset:29696
	ds_read_b128 v[74:77], v246 offset:30720
	ds_read_b128 v[78:81], v246 offset:31744
	v_mfma_f32_32x32x16_f16 v[98:113], v[50:53], v[4:7], v[98:113]
	v_exp_f32_e32 v114, v114
	v_exp_f32_e32 v115, v115
	v_exp_f32_e32 v116, v116
	v_exp_f32_e32 v117, v117
	v_exp_f32_e32 v118, v118
	v_exp_f32_e32 v119, v119
	v_exp_f32_e32 v120, v120
	v_exp_f32_e32 v121, v121
	v_mfma_f32_32x32x16_f16 v[98:113], v[54:57], v[8:11], v[98:113]
	v_exp_f32_e32 v122, v122
	v_exp_f32_e32 v123, v123
	v_exp_f32_e32 v124, v124
	v_exp_f32_e32 v125, v125
	v_exp_f32_e32 v126, v126
	v_exp_f32_e32 v127, v127
	v_exp_f32_e32 v128, v128
	v_exp_f32_e32 v129, v129
	v_mfma_f32_32x32x16_f16 v[98:113], v[58:61], v[12:15], v[98:113]
	v_add_f32_e32 v114, 1.0, v114
	v_add_f32_e32 v115, 1.0, v115
	v_add_f32_e32 v116, 1.0, v116
	v_add_f32_e32 v117, 1.0, v117
	v_add_f32_e32 v118, 1.0, v118
	v_add_f32_e32 v119, 1.0, v119
	v_add_f32_e32 v120, 1.0, v120
	v_add_f32_e32 v121, 1.0, v121
	v_add_f32_e32 v122, 1.0, v122
	v_add_f32_e32 v123, 1.0, v123
	v_add_f32_e32 v124, 1.0, v124
	v_add_f32_e32 v125, 1.0, v125
	v_add_f32_e32 v126, 1.0, v126
	v_add_f32_e32 v127, 1.0, v127
	v_add_f32_e32 v128, 1.0, v128
	v_add_f32_e32 v129, 1.0, v129
	v_mfma_f32_32x32x16_f16 v[98:113], v[62:65], v[252:255], v[98:113]
	v_rcp_f32_e32 v114, v114
	v_rcp_f32_e32 v115, v115
	v_rcp_f32_e32 v116, v116
	v_rcp_f32_e32 v117, v117
	v_rcp_f32_e32 v118, v118
	v_rcp_f32_e32 v119, v119
	v_rcp_f32_e32 v120, v120
	v_rcp_f32_e32 v121, v121
	v_rcp_f32_e32 v122, v122
	v_rcp_f32_e32 v123, v123
	v_rcp_f32_e32 v124, v124
	v_rcp_f32_e32 v125, v125
	v_rcp_f32_e32 v126, v126
	v_rcp_f32_e32 v127, v127
	v_rcp_f32_e32 v128, v128
	v_rcp_f32_e32 v129, v129
	s_waitcnt lgkmcnt(8)
	ds_read_b128 v[18:21], v247 offset:33664
	ds_read_b128 v[22:25], v247 offset:33680
	ds_read_b128 v[26:29], v247 offset:33696
	ds_read_b128 v[30:33], v247 offset:33712
	v_fmac_f32_e32 v3, v162, v114
	v_fmac_f32_e32 v16, v163, v115
	v_fmac_f32_e32 v17, v164, v116
	v_fmac_f32_e32 v3, v165, v117
	v_fmac_f32_e32 v16, v166, v118
	v_fmac_f32_e32 v17, v167, v119
	v_fmac_f32_e32 v3, v168, v120
	v_fmac_f32_e32 v16, v169, v121
	v_fmac_f32_e32 v17, v170, v122
	v_fmac_f32_e32 v3, v171, v123
	v_fmac_f32_e32 v16, v172, v124
	v_fmac_f32_e32 v17, v173, v125
	v_fmac_f32_e32 v3, v174, v126
	v_fmac_f32_e32 v16, v175, v127
	v_fmac_f32_e32 v17, v176, v128
	v_fmac_f32_e32 v3, v177, v129
	s_waitcnt lgkmcnt(4)
	ds_read_b128 v[146:149], v247 offset:33728
	ds_read_b128 v[150:153], v247 offset:33744
	ds_read_b128 v[154:157], v247 offset:33760
	ds_read_b128 v[158:161], v247 offset:33776
	v_mfma_f32_32x32x16_f16 v[82:97], v[66:69], v[4:7], v[82:97]
	v_exp_f32_e32 v98, v98
	v_exp_f32_e32 v99, v99
	v_exp_f32_e32 v100, v100
	v_exp_f32_e32 v101, v101
	v_exp_f32_e32 v102, v102
	v_exp_f32_e32 v103, v103
	v_exp_f32_e32 v104, v104
	v_exp_f32_e32 v105, v105
	v_mfma_f32_32x32x16_f16 v[82:97], v[70:73], v[8:11], v[82:97]
	v_exp_f32_e32 v106, v106
	v_exp_f32_e32 v107, v107
	v_exp_f32_e32 v108, v108
	v_exp_f32_e32 v109, v109
	v_exp_f32_e32 v110, v110
	v_exp_f32_e32 v111, v111
	v_exp_f32_e32 v112, v112
	v_exp_f32_e32 v113, v113
	v_mfma_f32_32x32x16_f16 v[82:97], v[74:77], v[12:15], v[82:97]
	v_add_f32_e32 v98, 1.0, v98
	v_add_f32_e32 v99, 1.0, v99
	v_add_f32_e32 v100, 1.0, v100
	v_add_f32_e32 v101, 1.0, v101
	v_add_f32_e32 v102, 1.0, v102
	v_add_f32_e32 v103, 1.0, v103
	v_add_f32_e32 v104, 1.0, v104
	v_add_f32_e32 v105, 1.0, v105
	v_add_f32_e32 v106, 1.0, v106
	v_add_f32_e32 v107, 1.0, v107
	v_add_f32_e32 v108, 1.0, v108
	v_add_f32_e32 v109, 1.0, v109
	v_add_f32_e32 v110, 1.0, v110
	v_add_f32_e32 v111, 1.0, v111
	v_add_f32_e32 v112, 1.0, v112
	v_add_f32_e32 v113, 1.0, v113
	v_mfma_f32_32x32x16_f16 v[82:97], v[78:81], v[252:255], v[82:97]
	v_rcp_f32_e32 v98, v98
	v_rcp_f32_e32 v99, v99
	v_rcp_f32_e32 v100, v100
	v_rcp_f32_e32 v101, v101
	v_rcp_f32_e32 v102, v102
	v_rcp_f32_e32 v103, v103
	v_rcp_f32_e32 v104, v104
	v_rcp_f32_e32 v105, v105
	v_rcp_f32_e32 v106, v106
	v_rcp_f32_e32 v107, v107
	v_rcp_f32_e32 v108, v108
	v_rcp_f32_e32 v109, v109
	v_rcp_f32_e32 v110, v110
	v_rcp_f32_e32 v111, v111
	v_rcp_f32_e32 v112, v112
	v_rcp_f32_e32 v113, v113
	s_waitcnt lgkmcnt(4)
	v_fmac_f32_e32 v3, v18, v98
	v_fmac_f32_e32 v16, v19, v99
	v_fmac_f32_e32 v17, v20, v100
	v_fmac_f32_e32 v3, v21, v101
	v_fmac_f32_e32 v16, v22, v102
	v_fmac_f32_e32 v17, v23, v103
	v_fmac_f32_e32 v3, v24, v104
	v_fmac_f32_e32 v16, v25, v105
	v_fmac_f32_e32 v17, v26, v106
	v_fmac_f32_e32 v3, v27, v107
	v_fmac_f32_e32 v16, v28, v108
	v_fmac_f32_e32 v17, v29, v109
	v_fmac_f32_e32 v3, v30, v110
	v_fmac_f32_e32 v16, v31, v111
	v_fmac_f32_e32 v17, v32, v112
	v_fmac_f32_e32 v3, v33, v113
	v_mov_b32_e32 v4, 0
	v_mov_b32_e32 v5, 0
	v_mov_b32_e32 v6, 0
	v_mov_b32_e32 v7, 0
	v_exp_f32_e32 v82, v82
	v_exp_f32_e32 v83, v83
	v_exp_f32_e32 v84, v84
	v_exp_f32_e32 v85, v85
	v_exp_f32_e32 v86, v86
	v_exp_f32_e32 v87, v87
	v_exp_f32_e32 v88, v88
	v_exp_f32_e32 v89, v89
	v_mfma_f32_32x32x16_f16 v[66:81], v[4:7], v[4:7], 0
	v_exp_f32_e32 v90, v90
	v_exp_f32_e32 v91, v91
	v_exp_f32_e32 v92, v92
	v_exp_f32_e32 v93, v93
	v_exp_f32_e32 v94, v94
	v_exp_f32_e32 v95, v95
	v_exp_f32_e32 v96, v96
	v_exp_f32_e32 v97, v97
	v_mfma_f32_32x32x16_f16 v[50:65], v[4:7], v[4:7], 0
	v_add_f32_e32 v82, 1.0, v82
	v_add_f32_e32 v83, 1.0, v83
	v_add_f32_e32 v84, 1.0, v84
	v_add_f32_e32 v85, 1.0, v85
	v_add_f32_e32 v86, 1.0, v86
	v_add_f32_e32 v87, 1.0, v87
	v_add_f32_e32 v88, 1.0, v88
	v_add_f32_e32 v89, 1.0, v89
	v_add_f32_e32 v90, 1.0, v90
	v_add_f32_e32 v91, 1.0, v91
	v_add_f32_e32 v92, 1.0, v92
	v_add_f32_e32 v93, 1.0, v93
	v_add_f32_e32 v94, 1.0, v94
	v_add_f32_e32 v95, 1.0, v95
	v_add_f32_e32 v96, 1.0, v96
	v_add_f32_e32 v97, 1.0, v97
	v_mfma_f32_32x32x16_f16 v[34:49], v[4:7], v[4:7], 0
	v_rcp_f32_e32 v82, v82
	v_rcp_f32_e32 v83, v83
	v_rcp_f32_e32 v84, v84
	v_rcp_f32_e32 v85, v85
	v_rcp_f32_e32 v86, v86
	v_rcp_f32_e32 v87, v87
	v_rcp_f32_e32 v88, v88
	v_rcp_f32_e32 v89, v89
	v_rcp_f32_e32 v90, v90
	v_rcp_f32_e32 v91, v91
	v_rcp_f32_e32 v92, v92
	v_rcp_f32_e32 v93, v93
	v_rcp_f32_e32 v94, v94
	v_rcp_f32_e32 v95, v95
	v_rcp_f32_e32 v96, v96
	v_rcp_f32_e32 v97, v97
	s_waitcnt lgkmcnt(0)
	v_mfma_f32_32x32x16_f16 v[18:33], v[4:7], v[4:7], 0
	v_fmac_f32_e32 v3, v146, v82
	v_fmac_f32_e32 v16, v147, v83
	v_fmac_f32_e32 v17, v148, v84
	v_fmac_f32_e32 v3, v149, v85
	v_fmac_f32_e32 v16, v150, v86
	v_fmac_f32_e32 v17, v151, v87
	v_fmac_f32_e32 v3, v152, v88
	v_fmac_f32_e32 v16, v153, v89
	v_fmac_f32_e32 v17, v154, v90
	v_fmac_f32_e32 v3, v155, v91
	v_fmac_f32_e32 v16, v156, v92
	v_fmac_f32_e32 v17, v157, v93
	v_fmac_f32_e32 v3, v158, v94
	v_fmac_f32_e32 v16, v159, v95
	v_fmac_f32_e32 v17, v160, v96
	v_fmac_f32_e32 v3, v161, v97
	v_add_f32_e32 v3, v3, v16
	v_add_f32_e32 v3, v3, v17
	ds_bpermute_b32 v4, v248, v3
	s_and_saveexec_b64 s[8:9], s[10:11]
	s_cbranch_execz .LBB1_156
	s_waitcnt vmcnt(0)
	v_mul_f32_e32 v5, 0x40549a78, v238
	v_exp_f32_e32 v5, v5
	s_waitcnt lgkmcnt(0)
	v_add_f32_e32 v3, v3, v4
	v_ashrrev_i32_e32 v7, 31, v235
	v_mov_b32_e32 v6, v235
	v_add_f32_e32 v3, v239, v3
	v_lshl_add_u64 v[6:7], v[6:7], 2, s[52:53]
	v_mul_f32_e32 v3, v5, v3
	global_store_dword v[6:7], v3, off
